# b6 + conservative s_nop 0 pads removed between packed-u16 count ops in the top-k threshold search loop
# speedup vs baseline: 1.0203x; 1.0050x over previous
.LBB0_1255:
	v_lshlrev_b32_e64 v68, v67, 1
	v_or_b32_e32 v68, v68, v66
	v_add_u32_e32 v69, -1, v68
	v_lshlrev_b32_e32 v70, 16, v69
	v_or_b32_e32 v69, v70, v69
	s_waitcnt lgkmcnt(0)
	v_pk_sub_u16 v70, v50, v69 clamp
	v_pk_sub_u16 v71, v51, v69 clamp
	v_pk_sub_u16 v72, v52, v69 clamp
	v_pk_sub_u16 v73, v53, v69 clamp
	v_pk_sub_u16 v74, v41, v69 clamp
	s_andn2_b64 vcc, exec, s[28:29]
	v_pk_min_u16 v70, v70, v101
	v_pk_min_u16 v71, v71, v101
	v_pk_min_u16 v72, v72, v101
	v_pk_min_u16 v73, v73, v101
	v_pk_min_u16 v74, v74, v101
	v_pk_add_u16 v70, v70, v71
	v_pk_add_u16 v71, v72, v73
	v_pk_sub_u16 v72, v39, v69 clamp
	v_pk_sub_u16 v73, v40, v69 clamp
	v_pk_add_u16 v70, v70, v71
	v_pk_sub_u16 v71, v38, v69 clamp
	v_pk_min_u16 v72, v72, v101
	v_pk_min_u16 v73, v73, v101
	v_pk_min_u16 v71, v71, v101
	v_pk_add_u16 v70, v95, v70
	v_pk_add_u16 v71, v71, v72
	v_pk_add_u16 v72, v73, v74
	v_pk_sub_u16 v73, v28, v69 clamp
	v_pk_sub_u16 v74, v29, v69 clamp
	v_pk_add_u16 v71, v71, v72
	v_pk_sub_u16 v72, v27, v69 clamp
	v_pk_min_u16 v73, v73, v101
	v_pk_min_u16 v74, v74, v101
	v_pk_add_u16 v70, v70, v71
	v_pk_sub_u16 v71, v26, v69 clamp
	v_pk_min_u16 v72, v72, v101
	v_pk_min_u16 v71, v71, v101
	v_pk_add_u16 v71, v71, v72
	v_pk_add_u16 v72, v73, v74
	v_pk_sub_u16 v73, v20, v69 clamp
	v_pk_sub_u16 v74, v21, v69 clamp
	v_pk_add_u16 v71, v71, v72
	v_pk_sub_u16 v72, v19, v69 clamp
	v_pk_min_u16 v73, v73, v101
	v_pk_min_u16 v74, v74, v101
	v_pk_add_u16 v70, v70, v71
	v_pk_sub_u16 v71, v18, v69 clamp
	v_pk_min_u16 v72, v72, v101
	v_pk_min_u16 v71, v71, v101
	v_pk_add_u16 v71, v71, v72
	v_pk_add_u16 v72, v73, v74
	v_pk_add_u16 v71, v71, v72
	v_cndmask_b32_e64 v72, 0, 1, s[28:29]
	v_cmp_ne_u32_e64 s[8:9], 1, v72
	v_pk_add_u16 v70, v70, v71
	s_cbranch_vccnz .LBB0_1254
	v_pk_sub_u16 v71, v58, v69 clamp
	v_pk_sub_u16 v72, v59, v69 clamp
	v_pk_sub_u16 v73, v60, v69 clamp
	v_pk_sub_u16 v74, v61, v69 clamp
	s_andn2_b64 vcc, exec, s[26:27]
	v_pk_min_u16 v71, v71, v101
	v_pk_min_u16 v72, v72, v101
	v_pk_min_u16 v73, v73, v101
	v_pk_min_u16 v74, v74, v101
	v_pk_add_u16 v71, v71, v72
	v_pk_add_u16 v72, v73, v74
	v_pk_sub_u16 v73, v48, v69 clamp
	v_pk_sub_u16 v74, v49, v69 clamp
	v_pk_add_u16 v71, v71, v72
	v_pk_sub_u16 v72, v47, v69 clamp
	v_pk_min_u16 v73, v73, v101
	v_pk_min_u16 v74, v74, v101
	v_pk_add_u16 v70, v70, v71
	v_pk_sub_u16 v71, v46, v69 clamp
	v_pk_min_u16 v72, v72, v101
	v_pk_min_u16 v71, v71, v101
	v_pk_add_u16 v71, v71, v72
	v_pk_add_u16 v72, v73, v74
	v_pk_sub_u16 v73, v36, v69 clamp
	v_pk_sub_u16 v74, v37, v69 clamp
	v_pk_add_u16 v71, v71, v72
	v_pk_sub_u16 v72, v35, v69 clamp
	v_pk_min_u16 v73, v73, v101
	v_pk_min_u16 v74, v74, v101
	v_pk_add_u16 v70, v70, v71
	v_pk_sub_u16 v71, v34, v69 clamp
	v_pk_min_u16 v72, v72, v101
	v_pk_min_u16 v71, v71, v101
	v_pk_add_u16 v71, v71, v72
	v_pk_add_u16 v72, v73, v74
	v_pk_sub_u16 v73, v24, v69 clamp
	v_pk_sub_u16 v74, v25, v69 clamp
	v_pk_add_u16 v71, v71, v72
	v_pk_sub_u16 v72, v23, v69 clamp
	v_pk_min_u16 v73, v73, v101
	v_pk_min_u16 v74, v74, v101
	v_pk_add_u16 v70, v70, v71
	v_pk_sub_u16 v71, v22, v69 clamp
	v_pk_min_u16 v72, v72, v101
	v_pk_min_u16 v71, v71, v101
	v_pk_add_u16 v71, v71, v72
	v_pk_add_u16 v72, v73, v74
	v_pk_add_u16 v71, v71, v72
	v_pk_add_u16 v70, v70, v71
	s_cbranch_vccnz .LBB0_1254
	v_pk_sub_u16 v71, v62, v69 clamp
	v_pk_sub_u16 v72, v63, v69 clamp
	v_pk_sub_u16 v73, v64, v69 clamp
	v_pk_sub_u16 v74, v65, v69 clamp
	s_andn2_b64 vcc, exec, s[2:3]
	v_pk_min_u16 v71, v71, v101
	v_pk_min_u16 v72, v72, v101
	v_pk_min_u16 v73, v73, v101
	v_pk_min_u16 v74, v74, v101
	v_pk_add_u16 v71, v71, v72
	v_pk_add_u16 v72, v73, v74
	v_pk_sub_u16 v73, v56, v69 clamp
	v_pk_sub_u16 v74, v57, v69 clamp
	v_pk_add_u16 v71, v71, v72
	v_pk_sub_u16 v72, v55, v69 clamp
	v_pk_min_u16 v73, v73, v101
	v_pk_min_u16 v74, v74, v101
	v_pk_add_u16 v70, v70, v71
	v_pk_sub_u16 v71, v54, v69 clamp
	v_pk_min_u16 v72, v72, v101
	v_pk_min_u16 v71, v71, v101
	v_pk_add_u16 v71, v71, v72
	v_pk_add_u16 v72, v73, v74
	v_pk_sub_u16 v73, v44, v69 clamp
	v_pk_sub_u16 v74, v45, v69 clamp
	v_pk_add_u16 v71, v71, v72
	v_pk_sub_u16 v72, v43, v69 clamp
	v_pk_min_u16 v73, v73, v101
	v_pk_min_u16 v74, v74, v101
	v_pk_add_u16 v70, v70, v71
	v_pk_sub_u16 v71, v42, v69 clamp
	v_pk_min_u16 v72, v72, v101
	v_pk_min_u16 v71, v71, v101
	v_pk_add_u16 v71, v71, v72
	v_pk_add_u16 v72, v73, v74
	v_pk_sub_u16 v73, v32, v69 clamp
	v_pk_sub_u16 v74, v33, v69 clamp
	v_pk_add_u16 v71, v71, v72
	v_pk_sub_u16 v72, v31, v69 clamp
	v_pk_min_u16 v73, v73, v101
	v_pk_min_u16 v74, v74, v101
	v_pk_add_u16 v70, v70, v71
	v_pk_sub_u16 v71, v30, v69 clamp
	v_pk_min_u16 v72, v72, v101
	v_pk_min_u16 v71, v71, v101
	v_pk_add_u16 v71, v71, v72
	v_pk_add_u16 v72, v73, v74
	v_pk_add_u16 v71, v71, v72
	v_pk_add_u16 v70, v70, v71
	s_cbranch_vccnz .LBB0_1254
	v_pk_sub_u16 v71, v14, v69 clamp
	v_pk_sub_u16 v72, v15, v69 clamp
	v_pk_sub_u16 v73, v16, v69 clamp
	v_pk_sub_u16 v74, v17, v69 clamp
	v_pk_min_u16 v71, v71, v101
	v_pk_min_u16 v72, v72, v101
	v_pk_min_u16 v73, v73, v101
	v_pk_min_u16 v74, v74, v101
	v_pk_add_u16 v71, v71, v72
	v_pk_add_u16 v72, v73, v74
	v_pk_sub_u16 v73, v12, v69 clamp
	v_pk_sub_u16 v74, v13, v69 clamp
	v_pk_add_u16 v71, v71, v72
	v_pk_sub_u16 v72, v11, v69 clamp
	v_pk_min_u16 v73, v73, v101
	v_pk_min_u16 v74, v74, v101
	v_pk_add_u16 v70, v70, v71
	v_pk_sub_u16 v71, v10, v69 clamp
	v_pk_min_u16 v72, v72, v101
	v_pk_min_u16 v71, v71, v101
	v_pk_add_u16 v71, v71, v72
	v_pk_add_u16 v72, v73, v74
	v_pk_sub_u16 v73, v8, v69 clamp
	v_pk_sub_u16 v74, v9, v69 clamp
	v_pk_add_u16 v71, v71, v72
	v_pk_sub_u16 v72, v7, v69 clamp
	v_pk_min_u16 v73, v73, v101
	v_pk_min_u16 v74, v74, v101
	v_pk_add_u16 v70, v70, v71
	v_pk_sub_u16 v71, v6, v69 clamp
	v_pk_min_u16 v72, v72, v101
	v_pk_min_u16 v71, v71, v101
	v_pk_add_u16 v71, v71, v72
	v_pk_add_u16 v72, v73, v74
	v_pk_sub_u16 v73, v4, v69 clamp
	v_pk_add_u16 v71, v71, v72
	v_pk_sub_u16 v72, v3, v69 clamp
	v_pk_min_u16 v73, v73, v101
	v_pk_add_u16 v70, v70, v71
	v_pk_sub_u16 v71, v2, v69 clamp
	v_pk_sub_u16 v69, v5, v69 clamp
	v_pk_min_u16 v72, v72, v101
	v_pk_min_u16 v69, v69, v101
	v_pk_min_u16 v71, v71, v101
	v_pk_add_u16 v69, v73, v69
	v_pk_add_u16 v71, v71, v72
	v_pk_add_u16 v69, v71, v69
	v_pk_add_u16 v70, v70, v69
	s_branch .LBB0_1254
.LBB0_1259:
	s_nop 0
	s_nop 0
	s_nop 0
	s_nop 0
	s_nop 0
	s_nop 0
	s_nop 0
	s_nop 0
	s_nop 0
	s_nop 0
	s_nop 0
	s_nop 0
	s_nop 0
	s_nop 0
	s_nop 0
	s_nop 0
	s_nop 0
	s_nop 0
	s_nop 0
	s_nop 0
	s_nop 0
	s_nop 0
	s_nop 0
	s_nop 0
	s_nop 0
	s_nop 0
	s_nop 0
	s_nop 0
	s_nop 0
	s_nop 0
	s_nop 0
	s_nop 0
	s_nop 0
	s_nop 0
	s_nop 0
	s_nop 0
	s_nop 0
	s_nop 0
	s_nop 0
	s_nop 0
	s_nop 0
	s_nop 0
	s_nop 0
	s_nop 0
	s_nop 0
	s_nop 0
	s_nop 0
	s_nop 0
	s_nop 0
	s_nop 0
	s_nop 0
	s_nop 0
	s_nop 0
	s_nop 0
	s_nop 0
	s_nop 0
	s_nop 0
	s_nop 0
	s_nop 0
	s_cmp_gt_i32 s14, 0
	s_cselect_b64 s[42:43], -1, 0
	s_cmp_lt_i32 s14, 1
	s_mov_b32 s4, 0
	s_cbranch_scc1 .LBB0_1277
	v_cmp_gt_u32_sdwa s[30:31], v50, v66 src0_sel:WORD_0 src1_sel:DWORD
	s_and_saveexec_b64 s[34:35], s[30:31]
	s_cbranch_execz .LBB0_1262
	v_and_b32_e32 v68, s30, v100
	v_and_b32_e32 v67, s31, v1
	v_bcnt_u32_b32 v68, v68, 0
	v_bcnt_u32_b32 v67, v67, v68
	v_lshl_add_u32 v67, v67, 1, s52
	ds_write_b16 v67, v119 offset:32768
